# v33 + work rebalance: pool-weight conversion, fp8 scale sampling (P0) and Wo fp8 tiles (P2) moved to the CUs with less strip/tile work
# baseline (speedup 1.0000x reference)
.LBB0_10:
	s_or_b64 exec, exec, s[2:3]
	s_load_dwordx2 s[92:93], s[0:1], 0x98
	s_waitcnt lgkmcnt(0)
	s_cmp_lt_i32 s92, 1
	s_cselect_b64 s[0:1], -1, 0
	s_cmp_gt_i32 s93, 0
	s_cselect_b64 s[2:3], -1, 0
	s_and_b64 s[14:15], s[0:1], s[2:3]
	s_andn2_b64 vcc, exec, s[14:15]
	s_cbranch_vccnz .LBB0_271
	s_lshr_b32 s100, s87, 1
	s_add_i32 s100, s90, s100
	s_cmp_ge_u32 s100, s87
	s_cselect_b32 s101, s87, 0
	s_sub_i32 s100, s100, s101
	s_add_i32 s0, 0, 0x23a48
	s_add_i32 s1, 0, 0x23a4c
	v_mov_b32_e32 v0, s0
	v_mov_b32_e32 v1, s1
	ds_read_b32 v0, v0
	ds_read_b32 v1, v1
	s_lshl_b32 s46, s89, 2
	s_cmp_gt_i32 s100, 63
	v_mbcnt_lo_u32_b32 v2, -1, 0
	v_mbcnt_hi_u32_b32 v2, -1, v2
	s_waitcnt lgkmcnt(1)
	v_readfirstlane_b32 s6, v0
	s_waitcnt lgkmcnt(0)
	v_readfirstlane_b32 s7, v1
	s_cbranch_scc1 .LBB0_14
	v_ashrrev_i32_e32 v0, 4, v2
	v_add_u32_e32 v5, s46, v0
	v_add_u32_e32 v6, s79, v2
	v_lshlrev_b32_e32 v3, 2, v2
	v_lshlrev_b32_e32 v2, 4, v2
	v_lshlrev_b32_e32 v0, 3, v5
	v_and_b32_e32 v4, 60, v3
	v_ashrrev_i32_e32 v6, 5, v6
	v_and_b32_e32 v2, 0x1f0, v2
	s_movk_i32 s0, 0x210
	s_add_u32 s8, s66, 0x600000
	v_ashrrev_i32_e32 v1, 31, v0
	v_mov_b32_e32 v3, 0
	v_lshl_add_u32 v7, v5, 4, 0
	v_add_u32_e32 v8, 0, v2
	v_mul_lo_u32 v9, v6, s0
	v_mul_u32_u24_e32 v10, 0x210, v4
	s_addc_u32 s9, s67, 0
	v_lshlrev_b64 v[0:1], 11, v[0:1]
	s_lshl_b32 s10, s100, 6
	s_lshl_b32 s11, s87, 6
	v_lshlrev_b32_e32 v4, 2, v4
	v_mov_b32_e32 v5, v3
	s_movk_i32 s12, 0x1000
	s_movk_i32 s13, 0x2000
	s_movk_i32 s16, 0x3000
	v_add_u32_e32 v7, v7, v10
	v_add_u32_e32 v8, v8, v9
	s_mov_b32 s17, s100

.LBB0_14:
	s_cmp_gt_i32 s100, 9
	v_mbcnt_lo_u32_b32 v2, -1, 0
	v_mbcnt_hi_u32_b32 v2, -1, v2
	s_cbranch_scc1 .LBB0_30
	s_cmp_lt_i32 s100, 8
	s_cselect_b64 s[0:1], -1, 0
	s_cmp_eq_u32 s100, 8
	s_cselect_b64 s[2:3], -1, 0
	s_cmp_lg_u32 s100, 8
	s_cselect_b64 s[4:5], -1, 0
	s_ashr_i32 s91, s90, 31
	s_ashr_i32 s101, s100, 31
	s_cmp_gt_i32 s100, 7
	s_cbranch_scc0 .LBB0_18
	s_and_b64 vcc, exec, s[4:5]
	s_cbranch_vccz .LBB0_19
	s_add_i32 s4, 0, 0x23a68
	v_mov_b32_e32 v0, s4
	s_add_i32 s4, 0, 0x23a6c
	v_mov_b32_e32 v1, s4
	ds_read_b32 v0, v0
	ds_read_b32 v1, v1
	s_waitcnt lgkmcnt(1)
	v_readfirstlane_b32 s4, v0
	s_waitcnt lgkmcnt(0)
	v_readfirstlane_b32 s5, v1
	s_cbranch_execz .LBB0_20
	s_branch .LBB0_21

.LBB0_22:
	s_add_i32 s4, 0, 0x23aa0
	v_mov_b32_e32 v0, s4
	s_add_i32 s4, 0, 0x23aa4
	ds_read_b32 v0, v0
	v_mov_b32_e32 v1, s4
	ds_read_b32 v1, v1
	s_mul_i32 s4, s100, 0x3800000
	s_mul_hi_i32 s5, s100, 0x3800000
	s_waitcnt lgkmcnt(1)
	v_readfirstlane_b32 s6, v0
	s_add_u32 s4, s6, s4
	s_waitcnt lgkmcnt(0)
	v_readfirstlane_b32 s7, v1
	s_addc_u32 s5, s7, s5

.LBB0_27:
	s_or_b64 exec, exec, s[0:1]
	v_cmp_eq_u32_e32 vcc, 0, v3
	s_waitcnt lgkmcnt(0)
	s_barrier
	s_and_saveexec_b64 s[0:1], vcc
	s_cbranch_execz .LBB0_29
	v_mov_b32_e32 v4, 0
	ds_read_b128 v[0:3], v4
	ds_read_b128 v[4:7], v4 offset:16
	s_lshl_b64 s[2:3], s[100:101], 2
	s_add_u32 s2, s66, s2
	s_addc_u32 s3, s67, s3
	s_waitcnt lgkmcnt(1)
	v_max_f32_e32 v1, v1, v1
	v_max_f32_e32 v0, v0, v0
	v_max_f32_e32 v0, v0, v1
	v_max3_f32 v0, v0, v2, v3
	s_waitcnt lgkmcnt(0)
	v_max3_f32 v0, v0, v4, v5
	v_max3_f32 v0, v0, v6, v7
	v_mov_b32_e32 v1, 0x380000
	v_readfirstlane_b32 s4, v0
	s_bfe_u32 s4, s4, 0x80017
	s_add_i32 s5, s4, 0xffffff05
	s_lshl_b32 s4, s4, 23
	s_sub_i32 s4, 0x81000000, s4
	s_cmp_gt_u32 s5, 0xffffff09
	v_mov_b32_e32 v0, s4
	s_cselect_b64 vcc, -1, 0
	v_cndmask_b32_e32 v0, 1.0, v0, vcc
	global_store_dword v1, v0, s[2:3]

.LBB0_423:
	s_lshr_b32 s100, s87, 1
	s_add_i32 s100, s90, s100
	s_cmp_ge_u32 s100, s87
	s_cselect_b32 s101, s87, 0
	s_sub_i32 s100, s100, s101
	s_add_i32 s2, s87, 0x7f
	s_cmpk_lt_i32 s100, 0x80
	s_cselect_b64 s[0:1], -1, 0
	s_add_i32 s3, 0, 0x23a68
	v_mov_b32_e32 v0, s3
	s_add_i32 s3, 0, 0x23a6c
	v_mov_b32_e32 v1, s3
	s_ashr_i32 s3, s2, 31
	s_abs_i32 s2, s2
	s_xor_b32 s3, s3, s7
	s_mul_hi_u32 s7, s2, s8
	s_mul_i32 s8, s7, s6
	s_sub_i32 s2, s2, s8
	s_add_i32 s8, s7, 1
	s_sub_i32 s11, s2, s6
	s_cmp_ge_u32 s2, s6
	s_cselect_b32 s7, s8, s7
	s_cselect_b32 s2, s11, s2
	s_add_i32 s8, s7, 1
	s_cmp_ge_u32 s2, s6
	s_cselect_b32 s2, s8, s7
	ds_read_b32 v0, v0
	ds_read_b32 v1, v1
	s_xor_b32 s2, s2, s3
	s_sub_i32 s6, s2, s3
	s_cmp_gt_i32 s6, 0
	s_cselect_b64 s[2:3], -1, 0
	s_and_b64 s[0:1], s[2:3], s[0:1]
	s_waitcnt lgkmcnt(1)
	v_readfirstlane_b32 s9, v0
	s_waitcnt lgkmcnt(0)
	v_readfirstlane_b32 s10, v1
	s_andn2_b64 vcc, exec, s[0:1]
	s_waitcnt vmcnt(11)
	v_mbcnt_lo_u32_b32 v52, -1, 0
	v_mbcnt_hi_u32_b32 v52, -1, v52
	s_cbranch_vccnz .LBB0_428
	s_add_u32 s7, s66, 0x380024
	s_addc_u32 s8, s67, 0
	s_ashr_i32 s0, s100, 31
	s_lshr_b32 s0, s0, 25
	s_add_i32 s1, s100, s0
	s_ashr_i32 s0, s1, 7
	s_and_b32 s1, s1, 0xff80
	s_sub_i32 s11, s100, s1
	s_bfe_i32 s1, s11, 0x80000
	s_bfe_u32 s1, s1, 0x5000a
	s_add_i32 s12, s11, s1
	s_bfe_i32 s1, s12, 0x80000
	s_and_b32 s12, s12, 0xe0
	s_sext_i32_i16 s1, s1
	s_sub_i32 s11, s11, s12
	s_lshr_b32 s2, s1, 5
	s_sext_i32_i8 s11, s11
	s_bfe_i64 s[2:3], s[2:3], 0x100000
	s_ashr_i32 s1, s0, 31
	s_lshl_b32 s12, s11, 6
	s_lshl_b64 s[2:3], s[2:3], 22
	s_lshl_b64 s[0:1], s[0:1], 24
	s_ashr_i32 s13, s12, 31
	v_and_b32_e32 v0, -16, v52
	s_add_u32 s2, s9, s2
	v_add_u32_e32 v54, s79, v0
	s_addc_u32 s3, s10, s3
	v_ashrrev_i32_e32 v55, 31, v54
	s_add_u32 s0, s2, s0
	v_lshlrev_b32_e32 v0, 2, v52
	v_lshlrev_b64 v[134:135], 13, v[54:55]
	s_addc_u32 s1, s3, s1
	v_and_b32_e32 v56, 60, v0
	v_lshl_add_u64 v[0:1], s[0:1], 0, v[134:135]
	v_mov_b32_e32 v133, 0
	v_lshl_add_u64 v[0:1], s[12:13], 2, v[0:1]
	v_lshlrev_b32_e32 v132, 2, v56
	v_lshl_add_u64 v[58:59], v[0:1], 0, v[132:133]
	s_mov_b32 s0, 0x1e000
	v_add_co_u32_e32 v0, vcc, s0, v58
	s_mov_b32 s0, 0x1c000
	s_nop 0
	v_addc_co_u32_e32 v1, vcc, 0, v59, vcc
	s_waitcnt vmcnt(9)
	v_add_co_u32_e32 v12, vcc, s0, v58
	s_mov_b32 s0, 0x1a000
	s_nop 0
	v_addc_co_u32_e32 v13, vcc, 0, v59, vcc
	v_add_co_u32_e32 v14, vcc, s0, v58
	s_mov_b32 s0, 0x18000
	s_nop 0
	v_addc_co_u32_e32 v15, vcc, 0, v59, vcc
	v_add_co_u32_e32 v20, vcc, s0, v58
	s_mov_b32 s0, 0x16000
	s_nop 0
	v_addc_co_u32_e32 v21, vcc, 0, v59, vcc
	v_add_co_u32_e32 v22, vcc, s0, v58
	s_mov_b32 s0, 0x14000
	s_nop 0
	v_addc_co_u32_e32 v23, vcc, 0, v59, vcc
	v_add_co_u32_e32 v28, vcc, s0, v58
	s_mov_b32 s0, 0x12000
	s_nop 0
	v_addc_co_u32_e32 v29, vcc, 0, v59, vcc
	v_add_co_u32_e32 v30, vcc, s0, v58
	s_mov_b32 s0, 0x10000
	s_nop 0
	v_addc_co_u32_e32 v31, vcc, 0, v59, vcc
	s_waitcnt vmcnt(8)
	v_add_co_u32_e32 v36, vcc, s0, v58
	s_mov_b32 s0, 0xe000
	s_nop 0
	v_addc_co_u32_e32 v37, vcc, 0, v59, vcc
	v_add_co_u32_e32 v38, vcc, s0, v58
	s_mov_b32 s0, 0xc000
	s_nop 0
	v_addc_co_u32_e32 v39, vcc, 0, v59, vcc
	v_add_co_u32_e32 v44, vcc, s0, v58
	s_mov_b32 s0, 0xa000
	s_nop 0
	v_addc_co_u32_e32 v45, vcc, 0, v59, vcc
	v_add_co_u32_e32 v46, vcc, s0, v58
	s_mov_b32 s0, 0x8000
	s_nop 0
	v_addc_co_u32_e32 v47, vcc, 0, v59, vcc
	v_add_co_u32_e32 v60, vcc, s0, v58
	s_movk_i32 s0, 0x6000
	s_nop 0
	v_addc_co_u32_e32 v61, vcc, 0, v59, vcc
	v_add_co_u32_e32 v62, vcc, s0, v58
	s_movk_i32 s0, 0x4000
	s_nop 0
	v_addc_co_u32_e32 v63, vcc, 0, v59, vcc
	v_add_co_u32_e32 v64, vcc, s0, v58
	s_movk_i32 s0, 0x2000
	s_nop 0
	v_addc_co_u32_e32 v65, vcc, 0, v59, vcc
	v_add_co_u32_e32 v66, vcc, s0, v58
	global_load_dwordx4 v[0:3], v[0:1], off nt
	s_nop 0
	global_load_dwordx4 v[4:7], v[12:13], off nt
	global_load_dwordx4 v[8:11], v[14:15], off nt
	s_nop 0
	global_load_dwordx4 v[12:15], v[20:21], off nt
	global_load_dwordx4 v[16:19], v[22:23], off nt
	s_nop 0
	global_load_dwordx4 v[20:23], v[28:29], off nt
	global_load_dwordx4 v[24:27], v[30:31], off nt
	s_nop 0
	global_load_dwordx4 v[28:31], v[36:37], off nt
	global_load_dwordx4 v[32:35], v[38:39], off nt
	s_nop 0
	global_load_dwordx4 v[36:39], v[44:45], off nt
	global_load_dwordx4 v[40:43], v[46:47], off nt
	s_nop 0
	global_load_dwordx4 v[44:47], v[60:61], off nt
	global_load_dwordx4 v[48:51], v[62:63], off nt
	v_addc_co_u32_e32 v67, vcc, 0, v59, vcc
	global_load_dwordx4 v[60:63], v[64:65], off nt
	global_load_dwordx4 v[72:75], v[66:67], off nt
	global_load_dwordx4 v[76:79], v[58:59], off nt
	v_add_u32_e32 v53, s79, v52
	v_lshlrev_b32_e32 v52, 4, v52
	v_and_b32_e32 v132, 0x1f0, v52
	v_ashrrev_i32_e32 v136, 5, v53
	v_lshl_add_u64 v[52:53], s[66:67], 0, v[132:133]
	s_mov_b64 s[0:1], 0x2000000
	v_lshl_add_u64 v[138:139], v[52:53], 0, s[0:1]
	s_movk_i32 s0, 0x210
	v_add_u32_e32 v54, 0, v54
	v_add_u32_e32 v55, 0, v132
	v_mul_u32_u24_e32 v52, 0x210, v56
	v_mul_lo_u32 v53, v136, s0
	v_add_u32_e32 v140, 16, v136
	v_add_u32_e32 v142, 32, v136
	v_add_u32_e32 v144, 48, v136
	v_lshlrev_b32_e32 v132, 2, v56
	v_add_u32_e32 v146, v54, v52
	v_add_u32_e32 v147, v55, v53
	v_ashrrev_i32_e32 v137, 31, v136
	v_ashrrev_i32_e32 v141, 31, v140
	v_ashrrev_i32_e32 v143, 31, v142
	v_ashrrev_i32_e32 v145, 31, v144
	s_mov_b32 s11, 1
	s_mov_b32 s12, 0xc3e00000
	v_mov_b32_e32 v148, 0x43e00000
	s_mov_b32 s3, s100
	s_waitcnt vmcnt(15)
	v_mov_b64_e32 v[126:127], v[2:3]
	s_waitcnt vmcnt(14)
	v_mov_b64_e32 v[122:123], v[6:7]
	s_waitcnt vmcnt(13)
	v_mov_b64_e32 v[118:119], v[10:11]
	s_waitcnt vmcnt(12)
	v_mov_b64_e32 v[114:115], v[14:15]
	s_waitcnt vmcnt(11)
	v_mov_b64_e32 v[110:111], v[18:19]
	s_waitcnt vmcnt(10)
	v_mov_b64_e32 v[106:107], v[22:23]
	s_waitcnt vmcnt(9)
	v_mov_b64_e32 v[102:103], v[26:27]
	s_waitcnt vmcnt(8)
	v_mov_b64_e32 v[98:99], v[30:31]
	s_waitcnt vmcnt(7)
	v_mov_b64_e32 v[94:95], v[34:35]
	s_waitcnt vmcnt(6)
	v_mov_b64_e32 v[90:91], v[38:39]
	s_waitcnt vmcnt(5)
	v_mov_b64_e32 v[86:87], v[42:43]
	s_waitcnt vmcnt(4)
	v_mov_b64_e32 v[82:83], v[46:47]
	s_waitcnt vmcnt(3)
	v_mov_b64_e32 v[70:71], v[50:51]
	s_waitcnt vmcnt(2)
	v_mov_b64_e32 v[66:67], v[62:63]
	s_waitcnt vmcnt(1)
	v_mov_b64_e32 v[56:57], v[72:73]
	s_waitcnt vmcnt(0)
	v_mov_b64_e32 v[52:53], v[76:77]
	v_mov_b64_e32 v[124:125], v[0:1]
	v_mov_b64_e32 v[120:121], v[4:5]
	v_mov_b64_e32 v[116:117], v[8:9]
	v_mov_b64_e32 v[112:113], v[12:13]
	v_mov_b64_e32 v[108:109], v[16:17]
	v_mov_b64_e32 v[104:105], v[20:21]
	v_mov_b64_e32 v[100:101], v[24:25]
	v_mov_b64_e32 v[96:97], v[28:29]
	v_mov_b64_e32 v[92:93], v[32:33]
	v_mov_b64_e32 v[88:89], v[36:37]
	v_mov_b64_e32 v[84:85], v[40:41]
	v_mov_b64_e32 v[80:81], v[44:45]
	v_mov_b64_e32 v[68:69], v[48:49]
	v_mov_b64_e32 v[64:65], v[60:61]
	v_mov_b64_e32 v[58:59], v[74:75]
	v_mov_b64_e32 v[54:55], v[78:79]
	s_branch .LBB0_426
